# hyena latent unit: x1 / x2 streams touched (unused loads) before the first FFT so their later reads hit L2
# baseline (speedup 1.0000x reference)
.LBB0_1051:
	v_add_u32_e32 v3, s3, v38
	v_ashrrev_i32_e32 v7, 6, v3
	v_lshlrev_b32_e32 v7, 5, v7
	v_add3_u32 v7, v136, v7, s5
	ds_read_b64 v[54:55], v7
	v_add_u32_e32 v7, 0x200, v3
	v_ashrrev_i32_e32 v7, 6, v7
	v_lshlrev_b32_e32 v7, 5, v7
	v_add3_u32 v7, v136, v7, s5
	s_waitcnt lgkmcnt(0)
	global_store_dwordx2 v[52:53], v[54:55], off
	ds_read_b64 v[54:55], v7 offset:4096
	v_add_u32_e32 v7, 0x400, v3
	v_ashrrev_i32_e32 v7, 6, v7
	v_lshlrev_b32_e32 v7, 5, v7
	v_add3_u32 v7, v136, v7, s5
	s_waitcnt lgkmcnt(0)
	global_store_dwordx2 v[50:51], v[54:55], off
	ds_read_b64 v[54:55], v7 offset:8192
	s_addk_i32 s3, 0x800
	v_lshl_add_u64 v[50:51], v[50:51], 0, s[88:89]
	v_lshl_add_u64 v[52:53], v[52:53], 0, s[88:89]
	s_waitcnt lgkmcnt(0)
	global_store_dwordx2 v[48:49], v[54:55], off
	v_add_u32_e32 v54, 0x600, v3
	v_ashrrev_i32_e32 v3, 6, v54
	v_lshlrev_b32_e32 v3, 5, v3
	v_add3_u32 v3, v136, v3, s5
	ds_read_b64 v[56:57], v3 offset:12288
	v_ashrrev_i32_e32 v55, 31, v54
	s_addk_i32 s5, 0x4000
	v_lshl_add_u64 v[54:55], v[54:55], 3, s[18:19]
	v_lshl_add_u64 v[48:49], v[48:49], 0, s[88:89]
	s_cmp_eq_u32 s5, 0x20000
	s_waitcnt lgkmcnt(0)
	global_store_dwordx2 v[54:55], v[56:57], off
	s_cbranch_scc0 .LBB0_1051
	s_movk_i32 s22, 0x200
	s_mov_b64 s[18:19], 0
	s_and_b64 vcc, exec, s[0:1]
	s_barrier
	s_cbranch_vccz .LBB0_1044
	s_mov_b32 s53, s63
	s_lshl_b64 s[0:1], s[52:53], 14
	v_writelane_b32 v255, s0, 58
	s_nop 1
	v_writelane_b32 v255, s1, 59
	s_lshl_b64 s[0:1], s[52:53], 16
	s_add_u32 s64, s34, s0
	s_addc_u32 s65, s35, s1
	v_lshl_add_u64 v[40:41], v[4:5], 2, s[64:65]
	global_load_dwordx2 v[42:43], v[40:41], off
	v_lshl_add_u64 v[40:41], v[36:37], 2, s[64:65]
	global_load_dwordx2 v[44:45], v[40:41], off
	v_lshl_add_u64 v[40:41], v[34:35], 2, s[64:65]
	global_load_dwordx2 v[46:47], v[40:41], off
	v_lshl_add_u64 v[40:41], v[32:33], 2, s[64:65]
	global_load_dwordx2 v[48:49], v[40:41], off
	v_lshl_add_u64 v[40:41], v[30:31], 2, s[64:65]
	global_load_dwordx2 v[50:51], v[40:41], off
	v_lshl_add_u64 v[40:41], v[28:29], 2, s[64:65]
	global_load_dwordx2 v[52:53], v[40:41], off
	v_lshl_add_u64 v[40:41], v[26:27], 2, s[64:65]
	global_load_dwordx2 v[54:55], v[40:41], off
	v_lshl_add_u64 v[40:41], v[24:25], 2, s[64:65]
	global_load_dwordx2 v[56:57], v[40:41], off
	v_lshl_add_u64 v[40:41], v[22:23], 2, s[64:65]
	global_load_dwordx2 v[58:59], v[40:41], off
	v_lshl_add_u64 v[40:41], v[20:21], 2, s[64:65]
	global_load_dwordx2 v[60:61], v[40:41], off
	v_lshl_add_u64 v[40:41], v[18:19], 2, s[64:65]
	global_load_dwordx2 v[62:63], v[40:41], off
	v_lshl_add_u64 v[40:41], v[16:17], 2, s[64:65]
	global_load_dwordx2 v[64:65], v[40:41], off
	v_lshl_add_u64 v[40:41], v[14:15], 2, s[64:65]
	global_load_dwordx2 v[66:67], v[40:41], off
	v_lshl_add_u64 v[40:41], v[12:13], 2, s[64:65]
	s_lshl_b64 s[0:1], s[52:53], 2
	v_readlane_b32 s3, v255, 56
	global_load_dwordx2 v[68:69], v[40:41], off
	v_lshl_add_u64 v[40:41], v[10:11], 2, s[64:65]
	s_add_u32 s0, s3, s0
	v_readlane_b32 s3, v255, 57
	global_load_dwordx2 v[70:71], v[40:41], off
	v_lshl_add_u64 v[40:41], v[8:9], 2, s[64:65]
	s_addc_u32 s1, s3, s1
	global_load_dwordx2 v[72:73], v[40:41], off
	s_nop 0
	global_load_dword v40, v99, s[0:1]
	global_load_dword v3, v99, s[0:1] offset:2048
	s_mov_b32 s0, 0
	s_mov_b32 s1, s0
	v_mov_b64_e32 v[74:75], s[0:1]
	s_waitcnt vmcnt(17)
	ds_write_b64 v80, v[42:43]
	ds_write_b64 v120, v[74:75]
	s_waitcnt vmcnt(16)
	ds_write_b64 v81, v[44:45] offset:4096
	ds_write_b64 v118, v[74:75]
	s_waitcnt vmcnt(15)
	ds_write_b64 v82, v[46:47] offset:8192
	ds_write_b64 v116, v[74:75]
	s_waitcnt vmcnt(14)
	ds_write_b64 v83, v[48:49] offset:12288
	ds_write_b64 v114, v[74:75]
	s_waitcnt vmcnt(13)
	ds_write_b64 v84, v[50:51] offset:16384
	ds_write_b64 v112, v[74:75]
	s_waitcnt vmcnt(12)
	ds_write_b64 v85, v[52:53] offset:20480
	ds_write_b64 v110, v[74:75]
	s_waitcnt vmcnt(11)
	ds_write_b64 v86, v[54:55] offset:24576
	ds_write_b64 v108, v[74:75]
	s_waitcnt vmcnt(10)
	ds_write_b64 v87, v[56:57] offset:28672
	ds_write_b64 v1, v[74:75]
	s_waitcnt vmcnt(9)
	ds_write_b64 v135, v[58:59] offset:32768
	ds_write_b64 v88, v[74:75]
	s_waitcnt vmcnt(8)
	ds_write_b64 v134, v[60:61] offset:36864
	ds_write_b64 v89, v[74:75]
	s_waitcnt vmcnt(7)
	ds_write_b64 v133, v[62:63] offset:40960
	ds_write_b64 v90, v[74:75]
	s_waitcnt vmcnt(6)
	ds_write_b64 v132, v[64:65] offset:45056
	ds_write_b64 v91, v[74:75]
	s_waitcnt vmcnt(5)
	ds_write_b64 v131, v[66:67] offset:49152
	ds_write_b64 v92, v[74:75]
	s_waitcnt vmcnt(4)
	ds_write_b64 v130, v[68:69] offset:53248
	ds_write_b64 v93, v[74:75]
	s_waitcnt vmcnt(3)
	ds_write_b64 v129, v[70:71] offset:57344
	ds_write_b64 v94, v[74:75]
	s_waitcnt vmcnt(2)
	ds_write_b64 v127, v[72:73] offset:61440
	ds_write_b64 v95, v[74:75]
	s_add_u32 s98, s64, 0x2000000
	s_addc_u32 s99, s65, 0
	v_lshl_add_u64 v[196:197], v[4:5], 2, s[98:99]
	global_load_dwordx2 v[198:199], v[196:197], off
	v_lshl_add_u64 v[196:197], v[36:37], 2, s[98:99]
	global_load_dwordx2 v[198:199], v[196:197], off
	v_lshl_add_u64 v[196:197], v[34:35], 2, s[98:99]
	global_load_dwordx2 v[198:199], v[196:197], off
	v_lshl_add_u64 v[196:197], v[32:33], 2, s[98:99]
	global_load_dwordx2 v[198:199], v[196:197], off
	v_lshl_add_u64 v[196:197], v[30:31], 2, s[98:99]
	global_load_dwordx2 v[198:199], v[196:197], off
	v_lshl_add_u64 v[196:197], v[28:29], 2, s[98:99]
	global_load_dwordx2 v[198:199], v[196:197], off
	v_lshl_add_u64 v[196:197], v[26:27], 2, s[98:99]
	global_load_dwordx2 v[198:199], v[196:197], off
	v_lshl_add_u64 v[196:197], v[24:25], 2, s[98:99]
	global_load_dwordx2 v[198:199], v[196:197], off
	v_lshl_add_u64 v[196:197], v[22:23], 2, s[98:99]
	global_load_dwordx2 v[198:199], v[196:197], off
	v_lshl_add_u64 v[196:197], v[20:21], 2, s[98:99]
	global_load_dwordx2 v[198:199], v[196:197], off
	v_lshl_add_u64 v[196:197], v[18:19], 2, s[98:99]
	global_load_dwordx2 v[198:199], v[196:197], off
	v_lshl_add_u64 v[196:197], v[16:17], 2, s[98:99]
	global_load_dwordx2 v[198:199], v[196:197], off
	v_lshl_add_u64 v[196:197], v[14:15], 2, s[98:99]
	global_load_dwordx2 v[198:199], v[196:197], off
	v_lshl_add_u64 v[196:197], v[12:13], 2, s[98:99]
	global_load_dwordx2 v[198:199], v[196:197], off
	v_lshl_add_u64 v[196:197], v[10:11], 2, s[98:99]
	global_load_dwordx2 v[198:199], v[196:197], off
	v_lshl_add_u64 v[196:197], v[8:9], 2, s[98:99]
	global_load_dwordx2 v[198:199], v[196:197], off
	s_add_u32 s98, s64, 0x4000000
	s_addc_u32 s99, s65, 0
	v_lshl_add_u64 v[196:197], v[4:5], 2, s[98:99]
	global_load_dwordx2 v[198:199], v[196:197], off
	v_lshl_add_u64 v[196:197], v[36:37], 2, s[98:99]
	global_load_dwordx2 v[198:199], v[196:197], off
	v_lshl_add_u64 v[196:197], v[34:35], 2, s[98:99]
	global_load_dwordx2 v[198:199], v[196:197], off
	v_lshl_add_u64 v[196:197], v[32:33], 2, s[98:99]
	global_load_dwordx2 v[198:199], v[196:197], off
	v_lshl_add_u64 v[196:197], v[30:31], 2, s[98:99]
	global_load_dwordx2 v[198:199], v[196:197], off
	v_lshl_add_u64 v[196:197], v[28:29], 2, s[98:99]
	global_load_dwordx2 v[198:199], v[196:197], off
	v_lshl_add_u64 v[196:197], v[26:27], 2, s[98:99]
	global_load_dwordx2 v[198:199], v[196:197], off
	v_lshl_add_u64 v[196:197], v[24:25], 2, s[98:99]
	global_load_dwordx2 v[198:199], v[196:197], off
	v_lshl_add_u64 v[196:197], v[22:23], 2, s[98:99]
	global_load_dwordx2 v[198:199], v[196:197], off
	v_lshl_add_u64 v[196:197], v[20:21], 2, s[98:99]
	global_load_dwordx2 v[198:199], v[196:197], off
	v_lshl_add_u64 v[196:197], v[18:19], 2, s[98:99]
	global_load_dwordx2 v[198:199], v[196:197], off
	v_lshl_add_u64 v[196:197], v[16:17], 2, s[98:99]
	global_load_dwordx2 v[198:199], v[196:197], off
	v_lshl_add_u64 v[196:197], v[14:15], 2, s[98:99]
	global_load_dwordx2 v[198:199], v[196:197], off
	v_lshl_add_u64 v[196:197], v[12:13], 2, s[98:99]
	global_load_dwordx2 v[198:199], v[196:197], off
	v_lshl_add_u64 v[196:197], v[10:11], 2, s[98:99]
	global_load_dwordx2 v[198:199], v[196:197], off
	v_lshl_add_u64 v[196:197], v[8:9], 2, s[98:99]
	global_load_dwordx2 v[198:199], v[196:197], off
	s_waitcnt lgkmcnt(0)
	s_barrier
